# speedup vs baseline: 1.0139x; 1.0082x over previous
_Z10ode_kernelPKfPKDF16_S2_PfPKi:
	v_lshrrev_b32_e32 v167, 6, v0
	s_lshr_b32 s3, s2, 3
	v_add_u32_e32 v2, s3, v167
	s_load_dwordx4 s[4:7], s[0:1], 0x0
	s_load_dwordx2 s[12:13], s[0:1], 0x10
	v_and_b32_e32 v130, 3, v2
	v_and_b32_e32 v1, 63, v0
	v_readfirstlane_b32 s3, v130
	v_lshlrev_b32_e32 v166, 4, v1
	s_lshl_b32 s11, s3, 14
	v_lshl_or_b32 v2, v130, 17, v166
	v_mov_b32_e32 v3, 0
	s_and_b32 s17, s11, 0xc000
	s_mov_b32 s9, 0
	s_waitcnt lgkmcnt(0)
	v_lshl_add_u64 v[74:75], s[6:7], 0, v[2:3]
	s_lshl_b32 s8, s17, 1
	v_lshl_add_u64 v[46:47], v[74:75], 0, s[8:9]
	s_movk_i32 s15, 0x1000
	v_add_co_u32_e32 v18, vcc, s15, v46
	s_movk_i32 s14, 0x3000
	s_nop 0
	v_addc_co_u32_e32 v19, vcc, 0, v47, vcc
	v_add_co_u32_e32 v20, vcc, s14, v46
	s_lshl_b32 s10, s2, 10
	s_nop 0
	v_addc_co_u32_e32 v21, vcc, 0, v47, vcc
	s_and_b32 s8, s10, 0x3e000
	s_movk_i32 s16, 0x7000
	v_add_co_u32_e32 v48, vcc, s16, v46
	v_lshl_or_b32 v22, v1, 7, s8
	s_add_i32 s8, s11, 0x4000
	v_addc_co_u32_e32 v49, vcc, 0, v47, vcc
	s_movk_i32 s16, 0x5000
	s_and_b32 s8, s8, 0xc000
	v_add_co_u32_e32 v50, vcc, s16, v46
	s_lshl_b32 s8, s8, 1
	global_load_dwordx4 v[34:37], v[18:19], off offset:2048
	global_load_dwordx4 v[14:17], v[20:21], off offset:2048
	global_load_dwordx4 v[6:9], v[20:21], off offset:1024
	global_load_dwordx4 v[2:5], v[18:19], off offset:1024
	global_load_dwordx4 v[42:45], v[18:19], off offset:3072
	global_load_dwordx4 v[38:41], v[20:21], off offset:3072
	v_addc_co_u32_e32 v51, vcc, 0, v47, vcc
	v_lshl_add_u64 v[72:73], v[74:75], 0, s[8:9]
	v_add_co_u32_e32 v106, vcc, s14, v72
	global_load_dwordx4 v[10:13], v[50:51], off offset:1024
	global_load_dwordx4 v[52:55], v[50:51], off offset:2048
	global_load_dwordx4 v[56:59], v[48:49], off offset:2048
	v_addc_co_u32_e32 v107, vcc, 0, v73, vcc
	v_add_co_u32_e32 v108, vcc, s15, v72
	global_load_dwordx4 v[60:63], v[50:51], off offset:3072
	global_load_dwordx4 v[64:67], v[48:49], off offset:3072
	global_load_ushort v198, v22, s[12:13]
	v_addc_co_u32_e32 v109, vcc, 0, v73, vcc
	global_load_dwordx4 v[68:71], v[108:109], off offset:2048
	global_load_dwordx4 v[78:81], v[106:107], off offset:2048
	global_load_dwordx4 v[82:85], v[106:107], off offset:3072
	global_load_dwordx4 v[86:89], v[108:109], off offset:3072
	s_add_i32 s8, s11, 0x6000
	s_movk_i32 s16, 0x2000
	s_and_b32 s8, s8, 0xe000
	v_add_co_u32_e32 v26, vcc, s16, v46
	s_lshl_b32 s8, s8, 1
	s_nop 0
	v_addc_co_u32_e32 v27, vcc, 0, v47, vcc
	v_lshl_add_u64 v[110:111], v[74:75], 0, s[8:9]
	v_add_co_u32_e32 v112, vcc, s14, v110
	global_load_dwordx4 a[0:3], v[46:47], off
	global_load_dwordx4 a[8:11], v[46:47], off offset:1024
	global_load_dwordx4 a[12:15], v[26:27], off offset:1024
	global_load_dwordx4 a[20:23], v[26:27], off offset:2048
	global_load_dwordx4 a[16:19], v[46:47], off offset:2048
	global_load_dwordx4 a[24:27], v[46:47], off offset:3072
	global_load_dwordx4 a[4:7], v[20:21], off offset:-4096
	global_load_dwordx4 v[22:25], v[20:21], off
	global_load_dwordx4 a[28:31], v[26:27], off offset:3072
	s_nop 0
	global_load_dwordx4 v[18:21], v[18:19], off
	v_addc_co_u32_e32 v113, vcc, 0, v111, vcc
	v_add_co_u32_e32 v114, vcc, s15, v110
	v_lshl_or_b32 v199, v167, 15, v166
	s_nop 0
	v_addc_co_u32_e32 v115, vcc, 0, v111, vcc
	global_load_dwordx4 v[26:29], v[114:115], off offset:1024
	global_load_dwordx4 v[90:93], v[114:115], off offset:2048
	global_load_dwordx4 v[30:33], v[112:113], off offset:1024
	global_load_dwordx4 v[94:97], v[112:113], off offset:2048
	global_load_dwordx4 v[98:101], v[114:115], off offset:3072
	global_load_dwordx4 v[102:105], v[112:113], off offset:3072
	s_movk_i32 s8, 0x6000
	s_load_dwordx2 s[6:7], s[0:1], 0x20
	v_lshlrev_b32_e32 v76, 1, v0
	v_and_b32_e32 v200, 7, v0
	v_and_b32_e32 v128, 64, v76
	v_and_b32_e32 v179, 15, v0
	v_bfe_u32 v201, v0, 4, 1
	v_mov_b32_e32 v196, 0x44444444
	global_load_dwordx4 a[44:47], v[48:49], off offset:-4096
	s_waitcnt vmcnt(31)
	ds_write_b128 v199, v[14:17] offset:1024
	v_add_co_u32_e32 v14, vcc, s8, v46
	s_movk_i32 s8, 0x4000
	s_nop 0
	v_addc_co_u32_e32 v15, vcc, 0, v47, vcc
	s_waitcnt vmcnt(28)
	ds_write_b128 v199, v[42:45] offset:2048
	v_add_co_u32_e32 v42, vcc, s8, v46
	ds_write_b128 v199, v[34:37]
	s_nop 0
	v_addc_co_u32_e32 v43, vcc, 0, v47, vcc
	s_waitcnt vmcnt(27)
	ds_write_b128 v199, v[38:41] offset:3072
	v_add_co_u32_e32 v44, vcc, s16, v72
	global_load_dwordx4 a[36:39], v[14:15], off offset:1024
	global_load_dwordx4 a[32:35], v[42:43], off offset:1024
	global_load_dwordx4 a[48:51], v[42:43], off offset:2048
	global_load_dwordx4 a[52:55], v[14:15], off offset:2048
	global_load_dwordx4 a[60:63], v[14:15], off offset:3072
	global_load_dwordx4 a[40:43], v[50:51], off offset:-4096
	global_load_dwordx4 v[34:37], v[50:51], off
	global_load_dwordx4 v[38:41], v[48:49], off
	s_nop 0
	global_load_dwordx4 v[14:17], v[48:49], off offset:1024
	s_waitcnt vmcnt(34)
	ds_write_b128 v199, v[52:55] offset:4096
	s_waitcnt vmcnt(33)
	ds_write_b128 v199, v[56:59] offset:5120
	v_addc_co_u32_e32 v45, vcc, 0, v73, vcc
	s_xor_b32 s8, s17, 0x8000
	global_load_dwordx4 a[68:71], v[106:107], off offset:-4096
	s_waitcnt vmcnt(33)
	ds_write_b128 v199, v[60:63] offset:6144
	s_waitcnt vmcnt(32)
	ds_write_b128 v199, v[64:67] offset:7168
	v_add_co_u32_e32 v58, vcc, s16, v110
	s_lshl_b32 s8, s8, 1
	global_load_dwordx4 a[56:59], v[42:43], off offset:3072
	global_load_dwordx4 a[64:67], v[72:73], off
	global_load_dwordx4 a[72:75], v[72:73], off offset:1024
	global_load_dwordx4 a[80:83], v[72:73], off offset:2048
	global_load_dwordx4 a[84:87], v[44:45], off offset:2048
	global_load_dwordx4 a[92:95], v[44:45], off offset:3072
	global_load_dwordx4 a[76:79], v[44:45], off offset:1024
	global_load_dwordx4 a[88:91], v[72:73], off offset:3072
	global_load_dwordx4 v[46:49], v[106:107], off
	global_load_dwordx4 v[54:57], v[106:107], off offset:1024
	s_nop 0
	global_load_dwordx4 v[42:45], v[108:109], off
	global_load_dwordx4 v[50:53], v[108:109], off offset:1024
	s_waitcnt vmcnt(42)
	ds_write_b128 v199, v[68:71] offset:8192
	s_waitcnt vmcnt(41)
	ds_write_b128 v199, v[78:81] offset:9216
	s_waitcnt vmcnt(39)
	ds_write_b128 v199, v[86:89] offset:10240
	ds_write_b128 v199, v[82:85] offset:11264
	v_addc_co_u32_e32 v59, vcc, 0, v111, vcc
	v_lshl_add_u64 v[78:79], v[74:75], 0, s[8:9]
	v_add_co_u32_e32 v84, vcc, s14, v78
	global_load_dwordx4 a[96:99], v[110:111], off
	global_load_dwordx4 a[104:107], v[110:111], off offset:1024
	global_load_dwordx4 a[108:111], v[58:59], off offset:1024
	global_load_dwordx4 a[116:119], v[58:59], off offset:2048
	global_load_dwordx4 a[112:115], v[110:111], off offset:2048
	global_load_dwordx4 a[120:123], v[110:111], off offset:3072
	global_load_dwordx4 a[100:103], v[112:113], off offset:-4096
	global_load_dwordx4 v[62:65], v[112:113], off
	global_load_dwordx4 a[124:127], v[58:59], off offset:3072
	s_nop 0
	global_load_dwordx4 v[58:61], v[114:115], off
	v_addc_co_u32_e32 v85, vcc, 0, v79, vcc
	v_add_co_u32_e32 v82, vcc, s15, v78
	s_add_i32 s8, s11, 0xa000
	s_nop 0
	v_addc_co_u32_e32 v83, vcc, 0, v79, vcc
	global_load_dwordx4 v[110:113], v[82:83], off offset:2048
	global_load_dwordx4 v[106:109], v[84:85], off offset:2048
	s_waitcnt vmcnt(39)
	ds_write_b128 v199, v[90:93] offset:12288
	s_waitcnt vmcnt(37)
	ds_write_b128 v199, v[94:97] offset:13312
	s_waitcnt vmcnt(36)
	ds_write_b128 v199, v[98:101] offset:14336
	s_waitcnt vmcnt(35)
	ds_write_b128 v199, v[102:105] offset:15360
	global_load_dwordx4 a[128:131], v[78:79], off
	global_load_dwordx4 a[132:135], v[84:85], off offset:-4096
	global_load_dwordx4 a[136:139], v[78:79], off offset:1024
	global_load_dwordx4 a[144:147], v[78:79], off offset:2048
	global_load_dwordx4 v[102:105], v[82:83], off offset:3072
	global_load_dwordx4 v[98:101], v[84:85], off offset:3072
	s_and_b32 s8, s8, 0xe000
	v_add_co_u32_e32 v80, vcc, s16, v78
	s_lshl_b32 s8, s8, 1
	s_nop 0
	v_addc_co_u32_e32 v81, vcc, 0, v79, vcc
	v_lshl_add_u64 v[122:123], v[74:75], 0, s[8:9]
	v_add_co_u32_e32 v124, vcc, s14, v122
	s_add_i32 s8, s11, 0xc000
	s_nop 0
	v_addc_co_u32_e32 v125, vcc, 0, v123, vcc
	v_add_co_u32_e32 v126, vcc, s15, v122
	s_and_b32 s8, s8, 0xc000
	s_nop 0
	v_addc_co_u32_e32 v127, vcc, 0, v123, vcc
	global_load_dwordx4 v[70:73], v[124:125], off offset:1024
	global_load_dwordx4 v[114:117], v[124:125], off offset:2048
	global_load_dwordx4 v[66:69], v[126:127], off offset:1024
	global_load_dwordx4 v[118:121], v[126:127], off offset:2048
	global_load_dwordx4 a[148:151], v[80:81], off offset:2048
	global_load_dwordx4 a[156:159], v[80:81], off offset:3072
	global_load_dwordx4 v[132:135], v[126:127], off offset:3072
	global_load_dwordx4 v[136:139], v[124:125], off offset:3072
	global_load_dwordx4 a[140:143], v[80:81], off offset:1024
	global_load_dwordx4 a[152:155], v[78:79], off offset:3072
	s_nop 0
	global_load_dwordx4 v[78:81], v[84:85], off
	global_load_dwordx4 v[86:89], v[84:85], off offset:1024
	s_lshl_b32 s8, s8, 1
	v_lshl_add_u64 v[164:165], v[74:75], 0, s[8:9]
	v_add_co_u32_e32 v176, vcc, s14, v164
	s_add_i32 s11, s11, 0xe000
	s_nop 0
	v_addc_co_u32_e32 v177, vcc, 0, v165, vcc
	v_add_co_u32_e32 v184, vcc, s15, v164
	s_and_b32 s8, s11, 0xe000
	s_nop 0
	v_addc_co_u32_e32 v185, vcc, 0, v165, vcc
	global_load_dwordx4 v[140:143], v[184:185], off offset:2048
	global_load_dwordx4 v[144:147], v[176:177], off offset:2048
	global_load_dwordx4 v[148:151], v[176:177], off offset:3072
	global_load_dwordx4 v[152:155], v[184:185], off offset:3072
	s_lshl_b32 s8, s8, 1
	v_lshl_add_u64 v[186:187], v[74:75], 0, s[8:9]
	v_add_co_u32_e32 v188, vcc, s14, v186
	v_and_or_b32 v74, v76, 16, v200
	s_nop 0
	v_addc_co_u32_e32 v189, vcc, 0, v187, vcc
	v_add_co_u32_e32 v190, vcc, s15, v186
	v_lshlrev_b32_e32 v129, 2, v74
	s_nop 0
	v_addc_co_u32_e32 v191, vcc, 0, v187, vcc
	global_load_dwordx4 v[94:97], v[188:189], off offset:1024
	global_load_dwordx4 v[156:159], v[188:189], off offset:2048
	global_load_dwordx4 v[90:93], v[190:191], off offset:1024
	global_load_dwordx4 v[160:163], v[190:191], off offset:2048
	global_load_dwordx4 v[172:175], v[188:189], off offset:3072
	global_load_dwordx4 v[180:183], v[190:191], off offset:3072
	s_waitcnt lgkmcnt(0)
	global_load_dword v131, v129, s[6:7]
	global_load_dwordx4 v[74:77], v[82:83], off
	s_nop 0
	global_load_dwordx4 v[82:85], v[82:83], off offset:1024
	s_waitcnt vmcnt(32)
	ds_write_b128 v199, v[110:113] offset:16384
	s_waitcnt vmcnt(31)
	ds_write_b128 v199, v[106:109] offset:17408
	v_lshlrev_b32_e32 v106, 7, v130
	v_or3_b32 v202, v106, v128, v179
	v_lshlrev_b32_e32 v106, 9, v201
	v_or_b32_e32 v107, 32, v129
	v_or3_b32 v106, v106, s10, v202
	global_load_dword v178, v129, s[6:7] offset:128
	global_load_dword v192, v107, s[6:7] offset:128
	global_load_dword v193, v129, s[6:7] offset:32
	v_ashrrev_i32_e32 v107, 31, v106
	v_lshl_add_u64 v[128:129], v[106:107], 2, s[4:5]
	global_load_dword v171, v[128:129], off
	s_waitcnt vmcnt(30)
	ds_write_b128 v199, v[102:105] offset:18432
	s_waitcnt vmcnt(29)
	ds_write_b128 v199, v[98:101] offset:19456
	v_add_co_u32_e32 v98, vcc, s16, v122
	s_mov_b32 s14, 0x45000000
	s_nop 0
	v_addc_co_u32_e32 v99, vcc, 0, v123, vcc
	global_load_dwordx4 a[160:163], v[122:123], off
	global_load_dwordx4 a[168:171], v[122:123], off offset:1024
	global_load_dwordx4 a[172:175], v[98:99], off offset:1024
	global_load_dwordx4 a[180:183], v[98:99], off offset:2048
	global_load_dwordx4 a[176:179], v[122:123], off offset:2048
	global_load_dwordx4 a[184:187], v[122:123], off offset:3072
	global_load_dword v170, v[128:129], off offset:64
	global_load_dwordx4 a[164:167], v[124:125], off offset:-4096
	global_load_dwordx4 v[102:105], v[124:125], off
	global_load_dwordx4 a[188:191], v[98:99], off offset:3072
	s_nop 0
	global_load_dwordx4 v[98:101], v[126:127], off
	s_waitcnt vmcnt(36)
	ds_write_b128 v199, v[118:121] offset:20480
	ds_write_b128 v199, v[114:117] offset:21504
	global_load_dword v169, v[128:129], off offset:128
	v_add_co_u32_e32 v106, vcc, s16, v164
	s_waitcnt vmcnt(34)
	ds_write_b128 v199, v[132:135] offset:22528
	s_waitcnt vmcnt(33)
	ds_write_b128 v199, v[136:139] offset:23552
	v_addc_co_u32_e32 v107, vcc, 0, v165, vcc
	global_load_dwordx4 a[192:195], v[164:165], off
	global_load_dwordx4 a[196:199], v[176:177], off offset:-4096
	global_load_dwordx4 a[200:203], v[164:165], off offset:1024
	global_load_dwordx4 a[208:211], v[164:165], off offset:2048
	global_load_dwordx4 a[212:215], v[106:107], off offset:2048
	global_load_dwordx4 a[220:223], v[106:107], off offset:3072
	global_load_dwordx4 a[204:207], v[106:107], off offset:1024
	global_load_dwordx4 a[216:219], v[164:165], off offset:3072
	global_load_dwordx4 v[110:113], v[176:177], off
	global_load_dwordx4 v[118:121], v[176:177], off offset:1024
	s_nop 0
	global_load_dwordx4 v[106:109], v[184:185], off
	global_load_dwordx4 v[114:117], v[184:185], off offset:1024
	global_load_dword v168, v[128:129], off offset:192
	v_add_co_u32_e32 v122, vcc, s16, v186
	v_and_b32_e32 v133, 32, v0
	s_nop 0
	v_addc_co_u32_e32 v123, vcc, 0, v187, vcc
	s_waitcnt vmcnt(41)
	ds_write_b128 v199, v[140:143] offset:24576
	s_waitcnt vmcnt(40)
	ds_write_b128 v199, v[144:147] offset:25600
	s_waitcnt vmcnt(38)
	ds_write_b128 v199, v[152:155] offset:26624
	ds_write_b128 v199, v[148:151] offset:27648
	global_load_dwordx4 a[224:227], v[186:187], off
	global_load_dwordx4 a[232:235], v[186:187], off offset:1024
	global_load_dwordx4 a[236:239], v[122:123], off offset:1024
	global_load_dwordx4 a[244:247], v[122:123], off offset:2048
	global_load_dwordx4 a[240:243], v[186:187], off offset:2048
	global_load_dwordx4 a[248:251], v[186:187], off offset:3072
	global_load_dwordx4 a[228:231], v[188:189], off offset:-4096
	global_load_dwordx4 v[126:129], v[188:189], off
	global_load_dwordx4 a[252:255], v[122:123], off offset:3072
	s_nop 0
	global_load_dwordx4 v[122:125], v[190:191], off
	v_lshlrev_b32_e32 v132, 2, v201
	v_lshl_or_b32 v130, v130, 6, v133
	v_lshrrev_b32_e32 v139, 1, v0
	v_and_b32_e32 v203, 24, v139
	s_waitcnt vmcnt(44)
	ds_write_b128 v199, v[160:163] offset:28672
	ds_write_b128 v199, v[156:159] offset:29696
	s_waitcnt vmcnt(42)
	ds_write_b128 v199, v[180:183] offset:30720
	ds_write_b128 v199, v[172:175] offset:31744
	s_waitcnt vmcnt(10) lgkmcnt(0)
	v_lshrrev_b32_e32 v222, 2, v131
	v_and_or_b32 v222, v222, 8, v132
	v_mul_u32_u24_e32 v222, 0x110, v222
	v_and_or_b32 v223, v131, 31, v130
	v_add_lshl_u32 v223, v223, v222, 1
	v_or_b32_e32 v204, 0x20000, v223
	v_lshrrev_b32_e32 v222, 2, v178
	v_and_or_b32 v222, v222, 8, v132
	v_mul_u32_u24_e32 v222, 0x110, v222
	v_and_or_b32 v223, v178, 31, v130
	v_add_lshl_u32 v223, v223, v222, 1
	v_or_b32_e32 v205, 0x20000, v223
	v_lshrrev_b32_e32 v222, 2, v193
	v_and_or_b32 v222, v222, 8, v132
	v_mul_u32_u24_e32 v222, 0x110, v222
	v_and_or_b32 v223, v193, 31, v130
	v_add_lshl_u32 v223, v223, v222, 1
	v_or_b32_e32 v206, 0x20000, v223
	v_lshrrev_b32_e32 v222, 2, v192
	v_and_or_b32 v222, v222, 8, v132
	v_mul_u32_u24_e32 v222, 0x110, v222
	v_and_or_b32 v223, v192, 31, v130
	v_add_lshl_u32 v223, v223, v222, 1
	v_or_b32_e32 v207, 0x20000, v223
	s_movk_i32 s43, 0x110
	v_mad_u32_u24 v224, v179, s43, v203
	v_mov_b32_e32 v225, 0x20000
	v_lshl_or_b32 v224, v224, 1, v225
	s_lshl_b32 s43, s3, 1
	s_add_u32 s52, s43, 0
	s_and_b32 s52, s52, 7
	s_lshl_b32 s52, s52, 6
	s_nop 0
	v_add_u32_e32 v208, s52, v224
	s_add_u32 s52, s43, 1
	s_and_b32 s52, s52, 7
	s_lshl_b32 s52, s52, 6
	s_sub_u32 s52, s52, 64
	s_nop 0
	v_add_u32_e32 v209, s52, v224
	s_add_u32 s52, s43, 2
	s_and_b32 s52, s52, 7
	s_lshl_b32 s52, s52, 6
	s_nop 0
	v_add_u32_e32 v211, s52, v224
	s_add_u32 s52, s43, 3
	s_and_b32 s52, s52, 7
	s_lshl_b32 s52, s52, 6
	s_nop 0
	v_add_u32_e32 v212, s52, v224
	s_add_u32 s52, s43, 4
	s_and_b32 s52, s52, 7
	s_lshl_b32 s52, s52, 6
	s_nop 0
	v_add_u32_e32 v213, s52, v224
	s_add_u32 s52, s43, 5
	s_and_b32 s52, s52, 7
	s_lshl_b32 s52, s52, 6
	s_nop 0
	v_add_u32_e32 v214, s52, v224
	s_add_u32 s52, s43, 6
	s_and_b32 s52, s52, 7
	s_lshl_b32 s52, s52, 6
	s_nop 0
	v_add_u32_e32 v215, s52, v224
	s_add_u32 s52, s43, 7
	s_and_b32 s52, s52, 7
	s_lshl_b32 s52, s52, 6
	s_nop 0
	v_add_u32_e32 v216, s52, v224
	v_and_b32_e32 v225, 8, v0
	v_cmp_eq_u32_e32 vcc, 0, v225
	v_mov_b32_e32 v225, 0xeeeeeeee
	s_nop 1
	v_cndmask_b32_e32 v210, v225, v196, vcc
	v_and_b32_e32 v225, 47, v0
	v_cmp_eq_u32_e64 s[4:5], 0, v225
	v_lshlrev_b32_e32 v225, 4, v167
	v_lshlrev_b32_e32 v226, 3, v201
	s_mov_b32 s52, 0x24400
	v_or3_b32 v218, v225, v226, s52
	s_load_dwordx2 s[6:7], s[0:1], 0x18
	s_lshl_b32 s11, s2, 9
	s_mov_b64 s[22:23], 0
	s_mov_b32 s29, 0
	s_mov_b32 s30, 0
	v_mov_b32_e32 v221, 0
	s_mov_b32 s40, 0x3a000000
	s_mov_b32 s41, 0x34800000
	s_mov_b32 s42, 0x45000000
	v_mov_b32_e32 v217, 0x24480
	v_mov_b64_e32 v[230:231], 0
	v_mov_b64_e32 v[232:233], 0
	v_mov_b64_e32 v[234:235], 0
	v_mov_b64_e32 v[236:237], 0
	v_mov_b64_e32 v[238:239], 0
	v_mov_b64_e32 v[240:241], 0
	v_mov_b64_e32 v[242:243], 0
	v_mov_b64_e32 v[244:245], 0
	ds_write_b128 v217, v[230:233]
	v_mov_b32_e32 v178, 0
	v_fma_mixlo_f16 v131, v178, v238, v171
	v_fma_mixlo_f16 v139, v178, v238, v170
	v_fma_mixlo_f16 v147, v178, v238, v169
	v_fma_mixlo_f16 v155, v178, v238, v168
	v_fma_f32 v130, v178, v238, v171
	v_fma_f32 v138, v178, v238, v170
	v_fma_f32 v146, v178, v238, v169
	v_fma_f32 v154, v178, v238, v168
	v_fma_mix_f32 v130, v130, 1.0, -v131 op_sel_hi:[0,0,1]
	v_fma_mix_f32 v138, v138, 1.0, -v139 op_sel_hi:[0,0,1]
	v_fma_mix_f32 v146, v146, 1.0, -v147 op_sel_hi:[0,0,1]
	v_fma_mix_f32 v154, v154, 1.0, -v155 op_sel_hi:[0,0,1]
	v_fma_mixlo_f16 v133, v130, s42, 0
	v_fma_mixlo_f16 v141, v138, s42, 0
	v_fma_mixlo_f16 v149, v146, s42, 0
	v_fma_mixlo_f16 v157, v154, s42, 0
	v_fma_mix_f32 v130, v130, s42, -v133 op_sel_hi:[0,0,1]
	v_fma_mix_f32 v138, v138, s42, -v141 op_sel_hi:[0,0,1]
	v_fma_mix_f32 v146, v146, s42, -v149 op_sel_hi:[0,0,1]
	v_fma_mix_f32 v154, v154, s42, -v157 op_sel_hi:[0,0,1]
	v_fma_mixlo_f16 v132, v130, s42, 0
	v_fma_mixlo_f16 v140, v138, s42, 0
	v_fma_mixlo_f16 v148, v146, s42, 0
	v_fma_mixlo_f16 v156, v154, s42, 0
	ds_write_b16 v204, v131
	ds_write_b16 v205, v139
	ds_write_b16 v206, v147
	ds_write_b16 v207, v155
	ds_write_b16 v204, v133 offset:544
	ds_write_b16 v205, v141 offset:544
	ds_write_b16 v206, v149 offset:544
	ds_write_b16 v207, v157 offset:544
	ds_write_b16 v204, v132 offset:1088
	ds_write_b16 v205, v140 offset:1088
	ds_write_b16 v206, v148 offset:1088
	ds_write_b16 v207, v156 offset:1088
	ds_read_b128 v[180:183], v199 offset:0
	s_waitcnt lgkmcnt(6)
	ds_read_b128 v[184:187], v199 offset:1024
	ds_read_b128 v[188:191], v199 offset:4096
	ds_read_b128 v[192:195], v199 offset:5120
	ds_read_b128 v[222:225], v199 offset:8192
	ds_read_b128 v[226:229], v199 offset:9216
	s_mov_b32 s52, 0x3a83126f
	v_mov_b32_e32 v248, 0x358637bd
	s_waitcnt lgkmcnt(0)
	s_barrier
	ds_read_b128 v[130:133], v208
	ds_read_b128 v[134:137], v209 offset:64
	ds_read_b128 v[138:141], v211
	ds_read_b128 v[142:145], v212
	ds_read_b128 v[146:149], v213
	ds_read_b128 v[150:153], v214
	ds_read_b128 v[154:157], v215
	ds_read_b128 v[158:161], v216
	s_waitcnt lgkmcnt(7)
	v_smfmac_f32_16x16x64_f16 v[230:233], v[130:133], a[16:23], v210
	v_fma_f32 v179, |v171|, s52, v248
	v_fma_f32 v196, |v170|, s52, v248
	v_smfmac_f32_16x16x64_f16 v[234:237], v[130:133], v[180:187], v210
	ds_read_b128 v[180:183], v199 offset:12288
	ds_read_b128 v[184:187], v199 offset:13312
	v_fma_f32 v197, |v169|, s52, v248
	s_waitcnt lgkmcnt(8)
	v_smfmac_f32_16x16x64_f16 v[230:233], v[134:137], a[48:55], v210
	v_fma_f32 v198, |v168|, s52, v248
	v_smfmac_f32_16x16x64_f16 v[234:237], v[134:137], v[188:195], v210
	ds_read_b128 v[188:191], v199 offset:16384
	ds_read_b128 v[192:195], v199 offset:17408
	v_rcp_f32_e32 v179, v179
	s_waitcnt lgkmcnt(9)
	v_smfmac_f32_16x16x64_f16 v[230:233], v[138:141], a[80:87], v210
	v_rcp_f32_e32 v196, v196
	v_smfmac_f32_16x16x64_f16 v[234:237], v[138:141], v[222:229], v210
	ds_read_b128 v[222:225], v199 offset:20480
	ds_read_b128 v[226:229], v199 offset:21504
	v_rcp_f32_e32 v197, v197
	s_waitcnt lgkmcnt(10)
	v_smfmac_f32_16x16x64_f16 v[230:233], v[142:145], a[112:119], v210
	v_rcp_f32_e32 v198, v198
	s_waitcnt lgkmcnt(4)
	v_smfmac_f32_16x16x64_f16 v[234:237], v[142:145], v[180:187], v210
	ds_read_b128 v[180:183], v199 offset:24576
	ds_read_b128 v[184:187], v199 offset:25600
	v_mul_f32_e32 v249, v170, v196
	v_smfmac_f32_16x16x64_f16 v[230:233], v[146:149], a[144:151], v210
	v_mul_f32_e32 v166, v249, v249
	s_waitcnt lgkmcnt(4)
	v_smfmac_f32_16x16x64_f16 v[234:237], v[146:149], v[188:195], v210
	ds_read_b128 v[188:191], v199 offset:28672
	ds_read_b128 v[192:195], v199 offset:29696
	v_mul_f32_e32 v249, v171, v179
	v_smfmac_f32_16x16x64_f16 v[230:233], v[150:153], a[176:183], v210
	v_fmac_f32_e32 v166, v249, v249
	s_waitcnt lgkmcnt(4)
	v_smfmac_f32_16x16x64_f16 v[234:237], v[150:153], v[222:229], v210
	ds_read_b128 v[222:225], v199 offset:2048
	ds_read_b128 v[226:229], v199 offset:3072
	v_mul_f32_e32 v249, v169, v197
	v_smfmac_f32_16x16x64_f16 v[230:233], v[154:157], a[208:215], v210
	v_fmac_f32_e32 v166, v249, v249
	s_waitcnt lgkmcnt(4)
	v_smfmac_f32_16x16x64_f16 v[234:237], v[154:157], v[180:187], v210
	ds_read_b128 v[180:183], v199 offset:6144
	ds_read_b128 v[184:187], v199 offset:7168
	v_mul_f32_e32 v249, v168, v198
	s_waitcnt vmcnt(0)
	v_smfmac_f32_16x16x64_f16 v[230:233], v[158:161], a[240:247], v210
	v_fmac_f32_e32 v166, v249, v249
	s_waitcnt lgkmcnt(4)
	v_smfmac_f32_16x16x64_f16 v[234:237], v[158:161], v[188:195], v210
	ds_read_b128 v[188:191], v199 offset:10240
	ds_read_b128 v[192:195], v199 offset:11264
	v_smfmac_f32_16x16x64_f16 v[238:241], v[130:133], a[24:31], v210
	s_waitcnt lgkmcnt(4)
	v_smfmac_f32_16x16x64_f16 v[242:245], v[130:133], v[222:229], v210
	ds_read_b128 v[222:225], v199 offset:14336
	ds_read_b128 v[226:229], v199 offset:15360
	v_smfmac_f32_16x16x64_f16 v[238:241], v[134:137], a[56:63], v210
	v_fmac_f32_e32 v230, s40, v231
	s_waitcnt lgkmcnt(4)
	v_smfmac_f32_16x16x64_f16 v[242:245], v[134:137], v[180:187], v210
	ds_read_b128 v[180:183], v199 offset:18432
	ds_read_b128 v[184:187], v199 offset:19456
	v_fmac_f32_e32 v234, s40, v235
	v_smfmac_f32_16x16x64_f16 v[238:241], v[138:141], a[88:95], v210
	v_fmac_f32_e32 v230, s41, v232
	s_waitcnt lgkmcnt(4)
	v_smfmac_f32_16x16x64_f16 v[242:245], v[138:141], v[188:195], v210
	ds_read_b128 v[188:191], v199 offset:22528
	ds_read_b128 v[192:195], v199 offset:23552
	v_fmac_f32_e32 v234, s41, v236
	v_smfmac_f32_16x16x64_f16 v[238:241], v[142:145], a[120:127], v210
	s_nop 0
	v_permlane32_swap_b32_e32 v230, v234
	s_waitcnt lgkmcnt(4)
	v_smfmac_f32_16x16x64_f16 v[242:245], v[142:145], v[222:229], v210
	ds_read_b128 v[222:225], v199 offset:26624
	ds_read_b128 v[226:229], v199 offset:27648
	v_add_f32_e32 v175, v230, v234
	v_smfmac_f32_16x16x64_f16 v[238:241], v[146:149], a[152:159], v210
	ds_read_b128 v[230:233], v217
	s_waitcnt lgkmcnt(5)
	v_smfmac_f32_16x16x64_f16 v[242:245], v[146:149], v[180:187], v210
	ds_read_b128 v[180:183], v199 offset:30720
	ds_read_b128 v[184:187], v199 offset:31744
	ds_read_b128 v[234:237], v217
	v_smfmac_f32_16x16x64_f16 v[238:241], v[150:153], a[184:191], v210
	s_waitcnt lgkmcnt(6)
	v_smfmac_f32_16x16x64_f16 v[242:245], v[150:153], v[188:195], v210
	v_smfmac_f32_16x16x64_f16 v[238:241], v[154:157], a[216:223], v210
	s_waitcnt lgkmcnt(4)
	v_smfmac_f32_16x16x64_f16 v[242:245], v[154:157], v[222:229], v210
	v_smfmac_f32_16x16x64_f16 v[238:241], v[158:161], a[248:255], v210
	s_waitcnt lgkmcnt(1)
	v_smfmac_f32_16x16x64_f16 v[242:245], v[158:161], v[180:187], v210
	v_smfmac_f32_16x16x64_f16 v[230:233], v[130:133], a[0:7], v210
	s_waitcnt lgkmcnt(0)
	v_smfmac_f32_16x16x64_f16 v[234:237], v[130:133], v[18:25], v210
	v_smfmac_f32_16x16x64_f16 v[230:233], v[134:137], a[40:47], v210
	v_fmac_f32_e32 v238, s40, v239
	v_smfmac_f32_16x16x64_f16 v[234:237], v[134:137], v[34:41], v210
	v_fmac_f32_e32 v242, s40, v243
	v_smfmac_f32_16x16x64_f16 v[230:233], v[138:141], a[64:71], v210
	v_fmac_f32_e32 v238, s41, v240
	v_smfmac_f32_16x16x64_f16 v[234:237], v[138:141], v[42:49], v210
	v_fmac_f32_e32 v242, s41, v244
	v_smfmac_f32_16x16x64_f16 v[230:233], v[142:145], a[96:103], v210
	s_nop 0
	v_permlane32_swap_b32_e32 v238, v242
	v_smfmac_f32_16x16x64_f16 v[234:237], v[142:145], v[58:65], v210
	v_add_f32_e32 v174, v238, v242
	v_smfmac_f32_16x16x64_f16 v[230:233], v[146:149], a[128:135], v210
	ds_read_b128 v[238:241], v217
	v_smfmac_f32_16x16x64_f16 v[234:237], v[146:149], v[74:81], v210
	ds_read_b128 v[242:245], v217
	v_smfmac_f32_16x16x64_f16 v[230:233], v[150:153], a[160:167], v210
	v_smfmac_f32_16x16x64_f16 v[234:237], v[150:153], v[98:105], v210
	v_smfmac_f32_16x16x64_f16 v[230:233], v[154:157], a[192:199], v210
	v_smfmac_f32_16x16x64_f16 v[234:237], v[154:157], v[106:113], v210
	v_smfmac_f32_16x16x64_f16 v[230:233], v[158:161], a[224:231], v210
	v_smfmac_f32_16x16x64_f16 v[234:237], v[158:161], v[122:129], v210
	s_waitcnt lgkmcnt(1)
	v_smfmac_f32_16x16x64_f16 v[238:241], v[130:133], a[8:15], v210
	s_waitcnt lgkmcnt(0)
	v_smfmac_f32_16x16x64_f16 v[242:245], v[130:133], v[2:9], v210
	v_smfmac_f32_16x16x64_f16 v[238:241], v[134:137], a[32:39], v210
	v_fmac_f32_e32 v230, s40, v231
	v_smfmac_f32_16x16x64_f16 v[242:245], v[134:137], v[10:17], v210
	v_fmac_f32_e32 v234, s40, v235
	v_smfmac_f32_16x16x64_f16 v[238:241], v[138:141], a[72:79], v210
	v_fmac_f32_e32 v230, s41, v232
	v_smfmac_f32_16x16x64_f16 v[242:245], v[138:141], v[50:57], v210
	v_fmac_f32_e32 v234, s41, v236
	v_smfmac_f32_16x16x64_f16 v[238:241], v[142:145], a[104:111], v210
	s_nop 0
	v_permlane32_swap_b32_e32 v230, v234
	v_smfmac_f32_16x16x64_f16 v[242:245], v[142:145], v[26:33], v210
	v_add_f32_e32 v173, v230, v234
	v_smfmac_f32_16x16x64_f16 v[238:241], v[146:149], a[136:143], v210
	ds_read_b128 v[230:233], v217
	v_smfmac_f32_16x16x64_f16 v[242:245], v[146:149], v[82:89], v210
	ds_read_b128 v[234:237], v217
	v_smfmac_f32_16x16x64_f16 v[238:241], v[150:153], a[168:175], v210
	v_smfmac_f32_16x16x64_f16 v[242:245], v[150:153], v[66:73], v210
	v_smfmac_f32_16x16x64_f16 v[238:241], v[154:157], a[200:207], v210
	v_smfmac_f32_16x16x64_f16 v[242:245], v[154:157], v[114:121], v210
	v_smfmac_f32_16x16x64_f16 v[238:241], v[158:161], a[232:239], v210
	v_smfmac_f32_16x16x64_f16 v[242:245], v[158:161], v[90:97], v210
	s_nop 6
	v_fmac_f32_e32 v238, s40, v239
	v_fmac_f32_e32 v242, s40, v243
	v_fmac_f32_e32 v238, s41, v240
	v_fmac_f32_e32 v242, s41, v244
	s_nop 1
	v_permlane32_swap_b32_e32 v238, v242
	v_add_f32_e32 v172, v238, v242
	ds_read_b128 v[180:183], v199 offset:0
	ds_read_b128 v[184:187], v199 offset:1024
	ds_read_b128 v[188:191], v199 offset:4096
	ds_read_b128 v[192:195], v199 offset:5120
	ds_read_b128 v[222:225], v199 offset:8192
	ds_read_b128 v[226:229], v199 offset:9216
	v_mul_f32_e32 v239, 0x3b000000, v172
	v_mul_f32_e32 v239, v239, v196
	v_mul_f32_e32 v167, v239, v239
	v_mul_f32_e32 v239, 0x3b000000, v173
	v_mul_f32_e32 v239, v239, v179
	v_fmac_f32_e32 v167, v239, v239
	v_mul_f32_e32 v239, 0x3b000000, v175
	v_mul_f32_e32 v239, v239, v197
	v_fmac_f32_e32 v167, v239, v239
	v_mul_f32_e32 v239, 0x3b000000, v174
	v_mul_f32_e32 v239, v239, v198
	v_fmac_f32_e32 v167, v239, v239
	v_mov_b32_e32 v130, v166
	v_mov_b32_e32 v131, v167
	s_nop 0
	v_add_f32_dpp v130, v130, v130 quad_perm:[1,0,3,2] row_mask:0xf bank_mask:0xf bound_ctrl:1
	v_add_f32_dpp v131, v131, v131 quad_perm:[1,0,3,2] row_mask:0xf bank_mask:0xf bound_ctrl:1
	s_nop 0
	v_add_f32_dpp v130, v130, v130 quad_perm:[2,3,0,1] row_mask:0xf bank_mask:0xf bound_ctrl:1
	v_add_f32_dpp v131, v131, v131 quad_perm:[2,3,0,1] row_mask:0xf bank_mask:0xf bound_ctrl:1
	s_nop 0
	v_add_f32_dpp v130, v130, v130 row_half_mirror row_mask:0xf bank_mask:0xf bound_ctrl:1
	v_add_f32_dpp v131, v131, v131 row_half_mirror row_mask:0xf bank_mask:0xf bound_ctrl:1
	s_nop 0
	v_add_f32_dpp v130, v130, v130 row_mirror row_mask:0xf bank_mask:0xf bound_ctrl:1
	v_add_f32_dpp v131, v131, v131 row_mirror row_mask:0xf bank_mask:0xf bound_ctrl:1
	v_mov_b32_e32 v240, v130
	v_mov_b32_e32 v241, v131
	s_nop 0
	v_permlane32_swap_b32_e32 v130, v240
	v_permlane32_swap_b32_e32 v131, v241
	v_add_f32_e32 v130, v130, v240
	v_add_f32_e32 v131, v131, v241
	v_add_u32_e32 v242, 0, v218
	v_lshlrev_b32_e32 v243, 3, v201
	v_or_b32_e32 v243, 0x24400, v243
	s_and_saveexec_b64 s[2:3], s[4:5]
	ds_write_b64 v242, v[130:131]
	s_or_b64 exec, exec, s[2:3]
	s_waitcnt lgkmcnt(0)
	s_barrier
	ds_read_b64 v[134:135], v243 offset:0
	ds_read_b64 v[138:139], v243 offset:16
	ds_read_b64 v[142:143], v243 offset:32
	ds_read_b64 v[146:147], v243 offset:48
	s_waitcnt lgkmcnt(2)
	v_add_f32_e32 v238, v134, v138
	s_waitcnt lgkmcnt(1)
	v_add_f32_e32 v238, v238, v142
	s_waitcnt lgkmcnt(0)
	v_add_f32_e32 v238, v238, v146
	v_add_f32_e32 v239, v135, v139
	v_add_f32_e32 v239, v239, v143
	v_add_f32_e32 v239, v239, v147
	v_mul_f32_e32 v238, 0x3b000000, v238
	v_max_f32_e32 v238, 0xda24260, v238
	v_sqrt_f32_e32 v238, v238
	v_mul_f32_e32 v239, 0x3b000000, v239
	v_max_f32_e32 v239, 0xda24260, v239
	v_sqrt_f32_e32 v239, v239
	s_nop 0
	v_mov_b32_e32 v220, v239
	v_rcp_f32_e32 v240, v239
	v_min_f32_e32 v241, v238, v239
	v_mul_f32_e32 v238, 0x3c23d70a, v238
	v_mul_f32_e32 v238, v238, v240
	s_mov_b32 s52, 0x3727c5ac
	v_cmp_ngt_f32_e32 vcc, s52, v241
	v_mov_b32_e32 v240, 0x358637bd
	s_nop 1
	v_cndmask_b32_e32 v219, v240, v238, vcc
	v_mul_f32_e32 v178, 0x3b000000, v219
	v_fma_mixlo_f16 v131, v178, v173, v171
	v_fma_mixlo_f16 v139, v178, v172, v170
	v_fma_mixlo_f16 v147, v178, v175, v169
	v_fma_mixlo_f16 v155, v178, v174, v168
	v_fma_f32 v130, v178, v173, v171
	v_fma_f32 v138, v178, v172, v170
	v_fma_f32 v146, v178, v175, v169
	v_fma_f32 v154, v178, v174, v168
	v_fma_mix_f32 v130, v130, 1.0, -v131 op_sel_hi:[0,0,1]
	v_fma_mix_f32 v138, v138, 1.0, -v139 op_sel_hi:[0,0,1]
	v_fma_mix_f32 v146, v146, 1.0, -v147 op_sel_hi:[0,0,1]
	v_fma_mix_f32 v154, v154, 1.0, -v155 op_sel_hi:[0,0,1]
	v_fma_mixlo_f16 v133, v130, s42, 0
	v_fma_mixlo_f16 v141, v138, s42, 0
	v_fma_mixlo_f16 v149, v146, s42, 0
	v_fma_mixlo_f16 v157, v154, s42, 0
	v_fma_mix_f32 v130, v130, s42, -v133 op_sel_hi:[0,0,1]
	v_fma_mix_f32 v138, v138, s42, -v141 op_sel_hi:[0,0,1]
	v_fma_mix_f32 v146, v146, s42, -v149 op_sel_hi:[0,0,1]
	v_fma_mix_f32 v154, v154, s42, -v157 op_sel_hi:[0,0,1]
	v_fma_mixlo_f16 v132, v130, s42, 0
	v_fma_mixlo_f16 v140, v138, s42, 0
	v_fma_mixlo_f16 v148, v146, s42, 0
	v_fma_mixlo_f16 v156, v154, s42, 0
	ds_write_b16 v204, v131 offset:8704
	ds_write_b16 v205, v139 offset:8704
	ds_write_b16 v206, v147 offset:8704
	ds_write_b16 v207, v155 offset:8704
	ds_write_b16 v204, v133 offset:9248
	ds_write_b16 v205, v141 offset:9248
	ds_write_b16 v206, v149 offset:9248
	ds_write_b16 v207, v157 offset:9248
	ds_write_b16 v204, v132 offset:9792
	ds_write_b16 v205, v140 offset:9792
	ds_write_b16 v206, v148 offset:9792
	ds_write_b16 v207, v156 offset:9792
	s_waitcnt lgkmcnt(0)
	s_barrier
	ds_read_b128 v[130:133], v208 offset:8704
	ds_read_b128 v[134:137], v209 offset:8768
	ds_read_b128 v[138:141], v211 offset:8704
	ds_read_b128 v[142:145], v212 offset:8704
	ds_read_b128 v[146:149], v213 offset:8704
	ds_read_b128 v[150:153], v214 offset:8704
	ds_read_b128 v[154:157], v215 offset:8704
	ds_read_b128 v[158:161], v216 offset:8704
	s_waitcnt lgkmcnt(7)
	v_smfmac_f32_16x16x64_f16 v[230:233], v[130:133], a[16:23], v210
	ds_read_b128 v[238:241], v217
	v_smfmac_f32_16x16x64_f16 v[234:237], v[130:133], v[180:187], v210
	ds_read_b128 v[180:183], v199 offset:12288
	ds_read_b128 v[184:187], v199 offset:13312
	ds_read_b128 v[242:245], v217
	s_waitcnt lgkmcnt(10)
	v_smfmac_f32_16x16x64_f16 v[230:233], v[134:137], a[48:55], v210
	v_smfmac_f32_16x16x64_f16 v[234:237], v[134:137], v[188:195], v210
	ds_read_b128 v[188:191], v199 offset:16384
	ds_read_b128 v[192:195], v199 offset:17408
	s_waitcnt lgkmcnt(11)
	v_smfmac_f32_16x16x64_f16 v[230:233], v[138:141], a[80:87], v210
	v_smfmac_f32_16x16x64_f16 v[234:237], v[138:141], v[222:229], v210
	ds_read_b128 v[222:225], v199 offset:20480
	ds_read_b128 v[226:229], v199 offset:21504
	s_waitcnt lgkmcnt(12)
	v_smfmac_f32_16x16x64_f16 v[230:233], v[142:145], a[112:119], v210
	s_waitcnt lgkmcnt(5)
	v_smfmac_f32_16x16x64_f16 v[234:237], v[142:145], v[180:187], v210
	ds_read_b128 v[180:183], v199 offset:24576
	ds_read_b128 v[184:187], v199 offset:25600
	v_smfmac_f32_16x16x64_f16 v[230:233], v[146:149], a[144:151], v210
	s_waitcnt lgkmcnt(4)
	v_smfmac_f32_16x16x64_f16 v[234:237], v[146:149], v[188:195], v210
	ds_read_b128 v[188:191], v199 offset:28672
	ds_read_b128 v[192:195], v199 offset:29696
	v_smfmac_f32_16x16x64_f16 v[230:233], v[150:153], a[176:183], v210
	s_waitcnt lgkmcnt(4)
	v_smfmac_f32_16x16x64_f16 v[234:237], v[150:153], v[222:229], v210
	ds_read_b128 v[222:225], v199 offset:2048
	ds_read_b128 v[226:229], v199 offset:3072
	v_smfmac_f32_16x16x64_f16 v[230:233], v[154:157], a[208:215], v210
	s_waitcnt lgkmcnt(4)
	v_smfmac_f32_16x16x64_f16 v[234:237], v[154:157], v[180:187], v210
	ds_read_b128 v[180:183], v199 offset:6144
	ds_read_b128 v[184:187], v199 offset:7168
	v_smfmac_f32_16x16x64_f16 v[230:233], v[158:161], a[240:247], v210
	s_waitcnt lgkmcnt(4)
	v_smfmac_f32_16x16x64_f16 v[234:237], v[158:161], v[188:195], v210
	ds_read_b128 v[188:191], v199 offset:10240
	ds_read_b128 v[192:195], v199 offset:11264
	v_smfmac_f32_16x16x64_f16 v[238:241], v[130:133], a[24:31], v210
	s_waitcnt lgkmcnt(4)
	v_smfmac_f32_16x16x64_f16 v[242:245], v[130:133], v[222:229], v210
	ds_read_b128 v[222:225], v199 offset:14336
	ds_read_b128 v[226:229], v199 offset:15360
	v_smfmac_f32_16x16x64_f16 v[238:241], v[134:137], a[56:63], v210
	v_fmac_f32_e32 v230, s40, v231
	s_waitcnt lgkmcnt(4)
	v_smfmac_f32_16x16x64_f16 v[242:245], v[134:137], v[180:187], v210
	ds_read_b128 v[180:183], v199 offset:18432
	ds_read_b128 v[184:187], v199 offset:19456
	v_fmac_f32_e32 v234, s40, v235
	v_smfmac_f32_16x16x64_f16 v[238:241], v[138:141], a[88:95], v210
	v_fmac_f32_e32 v230, s41, v232
	s_waitcnt lgkmcnt(4)
	v_smfmac_f32_16x16x64_f16 v[242:245], v[138:141], v[188:195], v210
	ds_read_b128 v[188:191], v199 offset:22528
	ds_read_b128 v[192:195], v199 offset:23552
	v_fmac_f32_e32 v234, s41, v236
	v_smfmac_f32_16x16x64_f16 v[238:241], v[142:145], a[120:127], v210
	s_nop 0
	v_permlane32_swap_b32_e32 v230, v234
	s_waitcnt lgkmcnt(4)
	v_smfmac_f32_16x16x64_f16 v[242:245], v[142:145], v[222:229], v210
	ds_read_b128 v[222:225], v199 offset:26624
	ds_read_b128 v[226:229], v199 offset:27648
	v_add_f32_e32 v164, v230, v234
	v_smfmac_f32_16x16x64_f16 v[238:241], v[146:149], a[152:159], v210
	ds_read_b128 v[230:233], v217
	s_waitcnt lgkmcnt(5)
	v_smfmac_f32_16x16x64_f16 v[242:245], v[146:149], v[180:187], v210
	ds_read_b128 v[180:183], v199 offset:30720
	ds_read_b128 v[184:187], v199 offset:31744
	ds_read_b128 v[234:237], v217
	v_smfmac_f32_16x16x64_f16 v[238:241], v[150:153], a[184:191], v210
	s_waitcnt lgkmcnt(6)
	v_smfmac_f32_16x16x64_f16 v[242:245], v[150:153], v[188:195], v210
	v_smfmac_f32_16x16x64_f16 v[238:241], v[154:157], a[216:223], v210
	s_waitcnt lgkmcnt(4)
	v_smfmac_f32_16x16x64_f16 v[242:245], v[154:157], v[222:229], v210
	v_smfmac_f32_16x16x64_f16 v[238:241], v[158:161], a[248:255], v210
	s_waitcnt lgkmcnt(1)
	v_smfmac_f32_16x16x64_f16 v[242:245], v[158:161], v[180:187], v210
	v_smfmac_f32_16x16x64_f16 v[230:233], v[130:133], a[0:7], v210
	s_waitcnt lgkmcnt(0)
	v_smfmac_f32_16x16x64_f16 v[234:237], v[130:133], v[18:25], v210
	v_smfmac_f32_16x16x64_f16 v[230:233], v[134:137], a[40:47], v210
	v_fmac_f32_e32 v238, s40, v239
	v_smfmac_f32_16x16x64_f16 v[234:237], v[134:137], v[34:41], v210
	v_fmac_f32_e32 v242, s40, v243
	v_smfmac_f32_16x16x64_f16 v[230:233], v[138:141], a[64:71], v210
	v_fmac_f32_e32 v238, s41, v240
	v_smfmac_f32_16x16x64_f16 v[234:237], v[138:141], v[42:49], v210
	v_fmac_f32_e32 v242, s41, v244
	v_smfmac_f32_16x16x64_f16 v[230:233], v[142:145], a[96:103], v210
	s_nop 0
	v_permlane32_swap_b32_e32 v238, v242
	v_smfmac_f32_16x16x64_f16 v[234:237], v[142:145], v[58:65], v210
	v_add_f32_e32 v165, v238, v242
	v_smfmac_f32_16x16x64_f16 v[230:233], v[146:149], a[128:135], v210
	ds_read_b128 v[238:241], v217
	v_smfmac_f32_16x16x64_f16 v[234:237], v[146:149], v[74:81], v210
	ds_read_b128 v[242:245], v217
	v_smfmac_f32_16x16x64_f16 v[230:233], v[150:153], a[160:167], v210
	v_smfmac_f32_16x16x64_f16 v[234:237], v[150:153], v[98:105], v210
	v_smfmac_f32_16x16x64_f16 v[230:233], v[154:157], a[192:199], v210
	v_smfmac_f32_16x16x64_f16 v[234:237], v[154:157], v[106:113], v210
	v_smfmac_f32_16x16x64_f16 v[230:233], v[158:161], a[224:231], v210
	v_smfmac_f32_16x16x64_f16 v[234:237], v[158:161], v[122:129], v210
	s_waitcnt lgkmcnt(1)
	v_smfmac_f32_16x16x64_f16 v[238:241], v[130:133], a[8:15], v210
	s_waitcnt lgkmcnt(0)
	v_smfmac_f32_16x16x64_f16 v[242:245], v[130:133], v[2:9], v210
	v_smfmac_f32_16x16x64_f16 v[238:241], v[134:137], a[32:39], v210
	v_fmac_f32_e32 v230, s40, v231
	v_smfmac_f32_16x16x64_f16 v[242:245], v[134:137], v[10:17], v210
	v_fmac_f32_e32 v234, s40, v235
	v_smfmac_f32_16x16x64_f16 v[238:241], v[138:141], a[72:79], v210
	v_fmac_f32_e32 v230, s41, v232
	v_smfmac_f32_16x16x64_f16 v[242:245], v[138:141], v[50:57], v210
	v_fmac_f32_e32 v234, s41, v236
	v_smfmac_f32_16x16x64_f16 v[238:241], v[142:145], a[104:111], v210
	s_nop 0
	v_permlane32_swap_b32_e32 v230, v234
	v_smfmac_f32_16x16x64_f16 v[242:245], v[142:145], v[26:33], v210
	v_add_f32_e32 v162, v230, v234
	v_smfmac_f32_16x16x64_f16 v[238:241], v[146:149], a[136:143], v210
	ds_read_b128 v[230:233], v217
	v_smfmac_f32_16x16x64_f16 v[242:245], v[146:149], v[82:89], v210
	ds_read_b128 v[234:237], v217
	v_smfmac_f32_16x16x64_f16 v[238:241], v[150:153], a[168:175], v210
	v_smfmac_f32_16x16x64_f16 v[242:245], v[150:153], v[66:73], v210
	v_smfmac_f32_16x16x64_f16 v[238:241], v[154:157], a[200:207], v210
	v_smfmac_f32_16x16x64_f16 v[242:245], v[154:157], v[114:121], v210
	v_smfmac_f32_16x16x64_f16 v[238:241], v[158:161], a[232:239], v210
	v_smfmac_f32_16x16x64_f16 v[242:245], v[158:161], v[90:97], v210
	s_nop 6
	v_fmac_f32_e32 v238, s40, v239
	v_fmac_f32_e32 v242, s40, v243
	v_fmac_f32_e32 v238, s41, v240
	v_fmac_f32_e32 v242, s41, v244
	s_nop 1
	v_permlane32_swap_b32_e32 v238, v242
	v_add_f32_e32 v163, v238, v242
	ds_read_b128 v[180:183], v199 offset:0
	ds_read_b128 v[184:187], v199 offset:1024
	ds_read_b128 v[188:191], v199 offset:4096
	ds_read_b128 v[192:195], v199 offset:5120
	ds_read_b128 v[222:225], v199 offset:8192
	ds_read_b128 v[226:229], v199 offset:9216
	v_sub_f32_e32 v238, v163, v172
	v_mul_f32_e32 v238, 0x3b000000, v238
	v_mul_f32_e32 v238, v238, v196
	v_mul_f32_e32 v130, v238, v238
	v_sub_f32_e32 v238, v162, v173
	v_mul_f32_e32 v238, 0x3b000000, v238
	v_mul_f32_e32 v238, v238, v179
	v_fmac_f32_e32 v130, v238, v238
	v_sub_f32_e32 v238, v164, v175
	v_mul_f32_e32 v238, 0x3b000000, v238
	v_mul_f32_e32 v238, v238, v197
	v_fmac_f32_e32 v130, v238, v238
	v_sub_f32_e32 v238, v165, v174
	v_mul_f32_e32 v238, 0x3b000000, v238
	v_mul_f32_e32 v238, v238, v198
	v_fmac_f32_e32 v130, v238, v238
	s_nop 1
	v_add_f32_dpp v130, v130, v130 quad_perm:[1,0,3,2] row_mask:0xf bank_mask:0xf bound_ctrl:1
	s_nop 1
	v_add_f32_dpp v130, v130, v130 quad_perm:[2,3,0,1] row_mask:0xf bank_mask:0xf bound_ctrl:1
	s_nop 1
	v_add_f32_dpp v130, v130, v130 row_half_mirror row_mask:0xf bank_mask:0xf bound_ctrl:1
	s_nop 1
	v_add_f32_dpp v130, v130, v130 row_mirror row_mask:0xf bank_mask:0xf bound_ctrl:1
	v_mov_b32_e32 v240, v130
	s_nop 1
	v_permlane32_swap_b32_e32 v130, v240
	v_add_f32_e32 v130, v130, v240
	v_add_u32_e32 v242, 64, v218
	v_lshlrev_b32_e32 v243, 3, v201
	v_or_b32_e32 v243, 0x24440, v243
	s_and_saveexec_b64 s[2:3], s[4:5]
	ds_write_b32 v242, v130
	s_or_b64 exec, exec, s[2:3]
	s_waitcnt lgkmcnt(0)
	s_barrier
	ds_read2_b32 v[134:135], v243 offset1:4
	ds_read2_b32 v[136:137], v243 offset0:8 offset1:12
	s_waitcnt lgkmcnt(1)
	v_add_f32_e32 v238, v134, v135
	s_waitcnt lgkmcnt(0)
	v_add_f32_e32 v238, v238, v136
	v_add_f32_e32 v238, v238, v137
	v_mul_f32_e32 v238, 0x3b000000, v238
	v_max_f32_e32 v238, 0xda24260, v238
	v_rcp_f32_e32 v240, v219
	v_sqrt_f32_e32 v238, v238
	s_nop 0
	v_mul_f32_e32 v238, v240, v238
	v_max_f32_e32 v241, v220, v238
	v_mul_f32_e32 v242, 0x3a83126f, v219
	v_max_f32_e32 v242, 0x358637bd, v242
	v_max_f32_e32 v243, 0x26901d7d, v241
	v_rcp_f32_e32 v243, v243
	s_nop 0
	v_mul_f32_e32 v243, 0x3c23d70a, v243
	v_log_f32_e32 v243, v243
	s_nop 0
	v_mul_f32_e32 v243, 0x3e4ccccd, v243
	v_exp_f32_e32 v243, v243
	s_mov_b32 s52, 0x26901d7d
	v_cmp_ge_f32_e32 vcc, s52, v241
	s_nop 1
	v_cndmask_b32_e32 v243, v243, v242, vcc
	v_mul_f32_e32 v242, 0x42c80000, v219
	v_min3_f32 v1, v242, v243, 1.0
	.p2align 6
